# final combine phases: nt (streaming) hint on the f32 output stores
# baseline (speedup 1.0000x reference)
; __device__ __forceinline__ float bflo(unsigned w) { return __uint_as_float(w << 16); }
; __device__ __forceinline__ float bfhi(unsigned w) { return __uint_as_float(w & 0xffff0000u); }
; __device__ __forceinline__ void p_final(const Args& a, const Frame& F, int half) {
;     ...
;     for (int t = tbeg + gw; t < tend; t += NGW) {
;         f32x4* xr = (f32x4*)(a.out + (size_t)t * D) + F.lane;
;         const u32x2* x1p = (const u32x2*)x1_row(a.out, a.ws, t) + F.lane;
;         const f32x4* g2 = (const f32x4*)(mod + (t >> 13) * 6144 + 5120) + F.lane;
;         int rk[4]; float wk[4];
; #pragma unroll
;         for (int k = 0; k < 4; ++k) { rk[k] = rkn[k]; wk[k] = wkn[k]; }
;         u32x2 ok[4][4], xw[4];
; #pragma unroll
;         for (int j = 0; j < 4; ++j) { xw[j] = x1p[64 * j];
; #pragma unroll
;             for (int k = 0; k < 4; ++k) ok[j][k] = *((const u32x2*)(OUTK + (size_t)rk[k] * D) + F.lane + 64 * j); }
;         { const int tn = t + NGW; if (tn < tend) {
; #pragma unroll
;             for (int k = 0; k < 4; ++k) { rkn[k] = tok_row[tn * 4 + k] - rowbase; wkn[k] = ent_w[tn * 4 + k]; } } }
;         f32x4 v[4]; float s = 0.f;
; #pragma unroll
;         for (int j = 0; j < 4; ++j) {
;             f32x4 m = (f32x4){0.f, 0.f, 0.f, 0.f};
; #pragma unroll
;             for (int k = 0; k < 4; ++k) { const u32x2 o = ok[j][k]; m.x += wk[k] * bflo(o.x); m.y += wk[k] * bfhi(o.x); m.z += wk[k] * bflo(o.y); m.w += wk[k] * bfhi(o.y); }
;             v[j] = (f32x4){bflo(xw[j].x), bfhi(xw[j].x), bflo(xw[j].y), bfhi(xw[j].y)} + g2[64 * j] * m;
;             s += (v[j].x * v[j].x + v[j].y * v[j].y) + (v[j].z * v[j].z + v[j].w * v[j].w);
;         }
.LBB0_1239:
	s_ashr_i32 s9, s4, 13
	s_mul_i32 s26, s9, 0x1800
	s_ashr_i32 s27, s26, 31
	s_lshl_b64 s[26:27], s[26:27], 2
	s_add_u32 s26, s72, s26
	s_addc_u32 s27, s73, s27
	v_lshlrev_b32_e32 v10, 4, v252
	v_lshl_add_u64 v[74:75], s[26:27], 0, v[10:11]
	v_add_co_u32_e32 v70, vcc, s24, v74
	v_lshl_add_u64 v[78:79], v[74:75], 0, s[12:13]
	s_nop 0
	v_addc_co_u32_e32 v71, vcc, 0, v75, vcc
	global_load_dwordx4 v[70:73], v[70:71], off
	s_waitcnt vmcnt(16)
	v_lshlrev_b32_e32 v80, 16, v54
	global_load_dwordx4 v[74:77], v[78:79], off offset:1024
	v_and_b32_e32 v81, 0xffff0000, v54
	v_lshlrev_b32_e32 v88, 16, v55
	v_and_b32_e32 v89, 0xffff0000, v55
	v_lshlrev_b32_e32 v90, 16, v52
	v_and_b32_e32 v91, 0xffff0000, v52
	v_lshlrev_b32_e32 v92, 16, v53
	v_and_b32_e32 v93, 0xffff0000, v53
	global_load_dwordx4 v[52:55], v[78:79], off offset:2048
	s_waitcnt vmcnt(17)
	v_lshlrev_b32_e32 v94, 16, v44
	v_and_b32_e32 v95, 0xffff0000, v44
	v_lshlrev_b32_e32 v44, 16, v45
	v_and_b32_e32 v45, 0xffff0000, v45
	v_lshlrev_b32_e32 v102, 16, v42
	v_and_b32_e32 v103, 0xffff0000, v42
	v_lshlrev_b32_e32 v104, 16, v43
	v_and_b32_e32 v105, 0xffff0000, v43
	s_waitcnt vmcnt(16)
	v_lshlrev_b32_e32 v42, 16, v34
	v_and_b32_e32 v43, 0xffff0000, v34
	v_pk_fma_f32 v[108:109], v[6:7], v[44:45], 0 op_sel_hi:[0,1,0]
	v_pk_fma_f32 v[110:111], v[6:7], v[42:43], 0 op_sel_hi:[0,1,0]
	global_load_dwordx4 v[42:45], v[78:79], off offset:3072
	s_waitcnt vmcnt(15)
	v_lshlrev_b32_e32 v82, 16, v56
	v_and_b32_e32 v83, 0xffff0000, v56
	v_lshlrev_b32_e32 v56, 16, v57
	v_and_b32_e32 v57, 0xffff0000, v57
	s_waitcnt vmcnt(14)
	v_lshlrev_b32_e32 v96, 16, v46
	v_and_b32_e32 v97, 0xffff0000, v46
	v_lshlrev_b32_e32 v46, 16, v47
	v_and_b32_e32 v47, 0xffff0000, v47
	v_pk_fma_f32 v[80:81], v[6:7], v[80:81], 0 op_sel_hi:[0,1,0]
	v_pk_fma_f32 v[88:89], v[6:7], v[88:89], 0 op_sel_hi:[0,1,0]
	v_pk_fma_f32 v[94:95], v[6:7], v[94:95], 0 op_sel_hi:[0,1,0]
	s_waitcnt vmcnt(11)
	v_lshlrev_b32_e32 v84, 16, v58
	v_and_b32_e32 v85, 0xffff0000, v58
	v_lshlrev_b32_e32 v58, 16, v59
	v_and_b32_e32 v59, 0xffff0000, v59
	s_waitcnt vmcnt(10)
	v_lshlrev_b32_e32 v98, 16, v48
	v_and_b32_e32 v99, 0xffff0000, v48
	v_lshlrev_b32_e32 v48, 16, v49
	v_and_b32_e32 v49, 0xffff0000, v49
	v_pk_fma_f32 v[80:81], v[6:7], v[82:83], v[80:81] op_sel:[1,0,0]
	v_pk_fma_f32 v[56:57], v[6:7], v[56:57], v[88:89] op_sel:[1,0,0]
	v_pk_fma_f32 v[78:79], v[6:7], v[96:97], v[94:95] op_sel:[1,0,0]
	v_pk_fma_f32 v[46:47], v[6:7], v[46:47], v[108:109] op_sel:[1,0,0]
	s_waitcnt vmcnt(7)
	v_lshlrev_b32_e32 v86, 16, v60
	v_and_b32_e32 v87, 0xffff0000, v60
	v_lshlrev_b32_e32 v60, 16, v61
	v_and_b32_e32 v61, 0xffff0000, v61
	s_waitcnt vmcnt(6)
	v_lshlrev_b32_e32 v100, 16, v50
	v_and_b32_e32 v101, 0xffff0000, v50
	v_lshlrev_b32_e32 v50, 16, v51
	v_and_b32_e32 v51, 0xffff0000, v51
	v_pk_fma_f32 v[80:81], v[8:9], v[84:85], v[80:81] op_sel_hi:[0,1,1]
	v_pk_fma_f32 v[56:57], v[8:9], v[58:59], v[56:57] op_sel_hi:[0,1,1]
	v_pk_fma_f32 v[58:59], v[8:9], v[98:99], v[78:79] op_sel_hi:[0,1,1]
	v_pk_fma_f32 v[46:47], v[8:9], v[48:49], v[46:47] op_sel_hi:[0,1,1]
	v_pk_fma_f32 v[48:49], v[8:9], v[86:87], v[80:81] op_sel:[1,0,0]
	v_pk_fma_f32 v[56:57], v[8:9], v[60:61], v[56:57] op_sel:[1,0,0]
	v_pk_fma_f32 v[58:59], v[8:9], v[100:101], v[58:59] op_sel:[1,0,0]
	v_pk_fma_f32 v[46:47], v[8:9], v[50:51], v[46:47] op_sel:[1,0,0]
	v_lshlrev_b32_e32 v34, 16, v35
	v_and_b32_e32 v35, 0xffff0000, v35
	v_lshlrev_b32_e32 v106, 16, v36
	v_and_b32_e32 v107, 0xffff0000, v36
	v_pk_fma_f32 v[34:35], v[6:7], v[34:35], 0 op_sel_hi:[0,1,0]
	v_lshlrev_b32_e32 v36, 16, v37
	v_and_b32_e32 v37, 0xffff0000, v37
	v_pk_fma_f32 v[34:35], v[6:7], v[36:37], v[34:35] op_sel:[1,0,0]
	v_lshlrev_b32_e32 v36, 16, v39
	v_and_b32_e32 v37, 0xffff0000, v39
	v_pk_fma_f32 v[34:35], v[8:9], v[36:37], v[34:35] op_sel_hi:[0,1,1]
	s_waitcnt vmcnt(5)
	v_lshlrev_b32_e32 v36, 16, v41
	v_and_b32_e32 v37, 0xffff0000, v41
	v_pk_fma_f32 v[34:35], v[8:9], v[36:37], v[34:35] op_sel:[1,0,0]
	v_lshlrev_b32_e32 v36, 16, v32
	v_and_b32_e32 v37, 0xffff0000, v32
	v_lshlrev_b32_e32 v32, 16, v33
	s_waitcnt vmcnt(3)
	v_pk_fma_f32 v[50:51], v[56:57], v[72:73], v[92:93]
	v_pk_fma_f32 v[48:49], v[48:49], v[70:71], v[90:91]
	s_waitcnt vmcnt(2)
	v_pk_fma_f32 v[46:47], v[46:47], v[76:77], v[104:105]
	v_pk_fma_f32 v[56:57], v[58:59], v[74:75], v[102:103]
	v_pk_mul_f32 v[58:59], v[48:49], v[48:49]
	v_pk_mul_f32 v[60:61], v[50:51], v[50:51]
	v_pk_mul_f32 v[70:71], v[46:47], v[46:47]
	v_pk_mul_f32 v[72:73], v[56:57], v[56:57]
	v_pk_mov_b32 v[74:75], v[58:59], v[60:61] op_sel:[1,0]
	v_mov_b32_e32 v59, v61
	v_pk_mov_b32 v[60:61], v[72:73], v[70:71] op_sel:[1,0]
	v_mov_b32_e32 v73, v71
	v_pk_add_f32 v[60:61], v[60:61], v[72:73]
	v_pk_fma_f32 v[70:71], v[6:7], v[106:107], v[110:111] op_sel:[1,0,0]
	v_lshlrev_b32_e32 v72, 16, v38
	v_and_b32_e32 v73, 0xffff0000, v38
	v_pk_fma_f32 v[70:71], v[8:9], v[72:73], v[70:71] op_sel_hi:[0,1,1]
	v_lshlrev_b32_e32 v72, 16, v40
	v_and_b32_e32 v73, 0xffff0000, v40
	v_pk_fma_f32 v[70:71], v[8:9], v[72:73], v[70:71] op_sel:[1,0,0]
	v_and_b32_e32 v33, 0xffff0000, v33
	s_waitcnt vmcnt(1)
; __device__ __forceinline__ float wave_sum(float v) {
; #pragma unroll
;     for (int o = 1; o < 64; o <<= 1) v += __shfl_xor(v, o);
;     return v;
; __device__ __forceinline__ void p_final(const Args& a, const Frame& F, int half) {
;     ...
;             s += (v[j].x * v[j].x + v[j].y * v[j].y) + (v[j].z * v[j].z + v[j].w * v[j].w);
;         }
;         const float rstd = rsqrtf(wave_sum(s) * (1.f / D) + EPS);
; #pragma unroll
;         for (int j = 0; j < 4; ++j) xr[64 * j] = v[j] * rstd * fw[64 * j];
	v_pk_fma_f32 v[32:33], v[34:35], v[54:55], v[32:33]
	v_pk_fma_f32 v[34:35], v[70:71], v[52:53], v[36:37]
	v_lshlrev_b32_e32 v36, 16, v28
	v_and_b32_e32 v37, 0xffff0000, v28
	v_pk_fma_f32 v[36:37], v[6:7], v[36:37], 0 op_sel_hi:[0,1,0]
	v_lshlrev_b32_e32 v38, 16, v30
	v_and_b32_e32 v39, 0xffff0000, v30
	v_pk_fma_f32 v[36:37], v[6:7], v[38:39], v[36:37] op_sel:[1,0,0]
	v_lshlrev_b32_e32 v38, 16, v24
	v_and_b32_e32 v39, 0xffff0000, v24
	v_pk_fma_f32 v[36:37], v[8:9], v[38:39], v[36:37] op_sel_hi:[0,1,1]
	v_lshlrev_b32_e32 v38, 16, v26
	v_and_b32_e32 v39, 0xffff0000, v26
	v_lshlrev_b32_e32 v28, 16, v29
	v_and_b32_e32 v29, 0xffff0000, v29
	v_pk_fma_f32 v[36:37], v[8:9], v[38:39], v[36:37] op_sel:[1,0,0]
	v_pk_fma_f32 v[38:39], v[6:7], v[28:29], 0 op_sel_hi:[0,1,0]
	v_lshlrev_b32_e32 v40, 16, v31
	v_and_b32_e32 v41, 0xffff0000, v31
	v_pk_fma_f32 v[6:7], v[6:7], v[40:41], v[38:39] op_sel:[1,0,0]
	v_lshlrev_b32_e32 v24, 16, v25
	v_and_b32_e32 v25, 0xffff0000, v25
	v_pk_fma_f32 v[6:7], v[8:9], v[24:25], v[6:7] op_sel_hi:[0,1,1]
	v_lshlrev_b32_e32 v24, 16, v27
	v_and_b32_e32 v25, 0xffff0000, v27
	v_pk_fma_f32 v[6:7], v[8:9], v[24:25], v[6:7] op_sel:[1,0,0]
	v_lshlrev_b32_e32 v8, 16, v22
	v_and_b32_e32 v9, 0xffff0000, v22
	v_pk_add_f32 v[58:59], v[74:75], v[58:59]
	v_lshlrev_b32_e32 v22, 16, v23
	v_and_b32_e32 v23, 0xffff0000, v23
	s_waitcnt vmcnt(0)
	v_pk_fma_f32 v[36:37], v[36:37], v[42:43], v[8:9]
	v_pk_fma_f32 v[26:27], v[6:7], v[44:45], v[22:23]
	v_mul_f32_e32 v8, v36, v36
	v_pk_add_f32 v[6:7], v[58:59], v[58:59] op_sel:[0,1] op_sel_hi:[1,0]
	v_mul_f32_e32 v10, v37, v37
	v_mov_b32_e32 v7, v8
	v_pk_add_f32 v[8:9], v[60:61], v[60:61] op_sel:[0,1] op_sel_hi:[1,0]
	v_mul_f32_e32 v22, v26, v26
	v_mov_b32_e32 v9, v10
	v_pk_add_f32 v[6:7], v[6:7], v[8:9]
	v_mul_f32_e32 v8, v35, v35
	v_pk_fma_f32 v[8:9], v[34:35], v[34:35], v[8:9] op_sel_hi:[1,1,0]
	v_mul_f32_e32 v10, v33, v33
	v_mul_f32_e32 v24, v27, v27
	v_mov_b32_e32 v9, v22
	v_pk_fma_f32 v[22:23], v[32:33], v[32:33], v[10:11] op_sel_hi:[1,1,0]
	s_add_u32 s4, s4, s6
	v_mov_b32_e32 v23, v24
	v_pk_add_f32 v[8:9], v[8:9], v[22:23]
	s_addc_u32 s5, s5, s7
	v_pk_add_f32 v[6:7], v[6:7], v[8:9]
	s_add_i32 s8, s8, s23
	v_add_f32_e32 v6, v6, v7
	s_cmp_lt_i32 s4, s14
	s_nop 1
	v_add_f32_dpp v6, v6, v6 row_ror:8 row_mask:0xf bank_mask:0xf bound_ctrl:1
	s_nop 1
	v_add_f32_dpp v6, v6, v6 row_ror:4 row_mask:0xf bank_mask:0xf bound_ctrl:1
	s_nop 1
	v_add_f32_dpp v6, v6, v6 row_ror:2 row_mask:0xf bank_mask:0xf bound_ctrl:1
	s_nop 1
	v_add_f32_dpp v6, v6, v6 row_ror:1 row_mask:0xf bank_mask:0xf bound_ctrl:1
	s_nop 1
	v_mov_b32_e32 v7, v6
	s_nop 1
	v_permlane16_swap_b32_e32 v6, v7
	s_nop 1
	v_add_f32_e32 v6, v6, v7
	v_mov_b32_e32 v7, v6
	s_nop 1
	v_permlane32_swap_b32_e32 v6, v7
	s_nop 1
	v_add_f32_e32 v6, v6, v7
	v_fmamk_f32 v6, v6, 0x3a800000, v68
	v_mul_f32_e32 v7, 0x4b800000, v6
	v_cmp_gt_f32_e32 vcc, s25, v6
	s_nop 1
	v_cndmask_b32_e32 v6, v6, v7, vcc
	v_rsq_f32_e32 v6, v6
	s_nop 0
	v_mul_f32_e32 v7, 0x45800000, v6
	v_cndmask_b32_e32 v10, v6, v7, vcc
	v_pk_mul_f32 v[6:7], v[48:49], v[10:11] op_sel_hi:[1,0]
	v_pk_mul_f32 v[8:9], v[50:51], v[10:11] op_sel_hi:[1,0]
	s_waitcnt vmcnt(0)
	v_pk_mul_f32 v[6:7], v[120:121], v[6:7]
	v_pk_mul_f32 v[8:9], v[122:123], v[8:9]
	global_store_dwordx4 v[16:17], v[6:9], off offset:-3072 nt
	v_pk_mul_f32 v[22:23], v[46:47], v[10:11] op_sel_hi:[1,0]
	v_pk_mul_f32 v[24:25], v[56:57], v[10:11] op_sel_hi:[1,0]
	v_pk_mul_f32 v[8:9], v[126:127], v[22:23]
	v_pk_mul_f32 v[6:7], v[124:125], v[24:25]
	global_store_dwordx4 v[16:17], v[6:9], off offset:-2048 nt
	v_pk_mul_f32 v[22:23], v[32:33], v[10:11] op_sel_hi:[1,0]
	v_pk_mul_f32 v[24:25], v[34:35], v[10:11] op_sel_hi:[1,0]
	v_pk_mul_f32 v[8:9], v[130:131], v[22:23]
	v_pk_mul_f32 v[6:7], v[128:129], v[24:25]
	global_store_dwordx4 v[16:17], v[6:9], off offset:-1024 nt
	s_nop 1
	v_mov_b64_e32 v[6:7], v[20:21]
	v_pk_mul_f32 v[8:9], v[26:27], v[10:11] op_sel_hi:[1,0]
	v_pk_mul_f32 v[20:21], v[36:37], v[10:11] op_sel_hi:[1,0]
	v_pk_mul_f32 v[20:21], v[132:133], v[20:21]
	v_pk_mul_f32 v[22:23], v[134:135], v[8:9]
	global_store_dwordx4 v[16:17], v[20:23], off nt
	v_lshl_add_u64 v[16:17], v[16:17], 0, s[10:11]
	v_mov_b64_e32 v[8:9], v[18:19]
	s_cbranch_scc0 .LBB0_1242

; __device__ __forceinline__ float bflo(unsigned w) { return __uint_as_float(w << 16); }
; __device__ __forceinline__ float bfhi(unsigned w) { return __uint_as_float(w & 0xffff0000u); }
; __device__ __forceinline__ void p_final(const Args& a, const Frame& F, int half) {
;     ...
;     for (int t = tbeg + gw; t < tend; t += NGW) {
;         f32x4* xr = (f32x4*)(a.out + (size_t)t * D) + F.lane;
;         const u32x2* x1p = (const u32x2*)x1_row(a.out, a.ws, t) + F.lane;
;         const f32x4* g2 = (const f32x4*)(mod + (t >> 13) * 6144 + 5120) + F.lane;
;         int rk[4]; float wk[4];
; #pragma unroll
;         for (int k = 0; k < 4; ++k) { rk[k] = rkn[k]; wk[k] = wkn[k]; }
;         u32x2 ok[4][4], xw[4];
; #pragma unroll
;         for (int j = 0; j < 4; ++j) { xw[j] = x1p[64 * j];
; #pragma unroll
;             for (int k = 0; k < 4; ++k) ok[j][k] = *((const u32x2*)(OUTK + (size_t)rk[k] * D) + F.lane + 64 * j); }
;         { const int tn = t + NGW; if (tn < tend) {
; #pragma unroll
;             for (int k = 0; k < 4; ++k) { rkn[k] = tok_row[tn * 4 + k] - rowbase; wkn[k] = ent_w[tn * 4 + k]; } } }
;         f32x4 v[4]; float s = 0.f;
; #pragma unroll
;         for (int j = 0; j < 4; ++j) {
;             f32x4 m = (f32x4){0.f, 0.f, 0.f, 0.f};
; #pragma unroll
;             for (int k = 0; k < 4; ++k) { const u32x2 o = ok[j][k]; m.x += wk[k] * bflo(o.x); m.y += wk[k] * bfhi(o.x); m.z += wk[k] * bflo(o.y); m.w += wk[k] * bfhi(o.y); }
;             v[j] = (f32x4){bflo(xw[j].x), bfhi(xw[j].x), bflo(xw[j].y), bfhi(xw[j].y)} + g2[64 * j] * m;
;             s += (v[j].x * v[j].x + v[j].y * v[j].y) + (v[j].z * v[j].z + v[j].w * v[j].w);
;         }
.LBB0_1395:
	s_ashr_i32 s7, s0, 13
	s_mul_i32 s22, s7, 0x1800
	s_ashr_i32 s23, s22, 31
	s_lshl_b64 s[22:23], s[22:23], 2
	s_add_u32 s22, s72, s22
	s_addc_u32 s23, s73, s23
	v_lshlrev_b32_e32 v4, 4, v252
	v_lshl_add_u64 v[74:75], s[22:23], 0, v[4:5]
	v_add_co_u32_e32 v70, vcc, s14, v74
	v_lshl_add_u64 v[78:79], v[74:75], 0, s[4:5]
	s_nop 0
	v_addc_co_u32_e32 v71, vcc, 0, v75, vcc
	global_load_dwordx4 v[70:73], v[70:71], off
	s_waitcnt vmcnt(16)
	v_lshlrev_b32_e32 v80, 16, v52
	global_load_dwordx4 v[74:77], v[78:79], off offset:1024
	v_and_b32_e32 v81, 0xffff0000, v52
	v_lshlrev_b32_e32 v88, 16, v53
	v_and_b32_e32 v89, 0xffff0000, v53
	v_lshlrev_b32_e32 v90, 16, v50
	v_and_b32_e32 v91, 0xffff0000, v50
	v_lshlrev_b32_e32 v92, 16, v51
	v_and_b32_e32 v93, 0xffff0000, v51
	global_load_dwordx4 v[50:53], v[78:79], off offset:2048
	s_waitcnt vmcnt(17)
	v_lshlrev_b32_e32 v94, 16, v42
	v_and_b32_e32 v95, 0xffff0000, v42
	v_lshlrev_b32_e32 v42, 16, v43
	v_and_b32_e32 v43, 0xffff0000, v43
	v_lshlrev_b32_e32 v102, 16, v40
	v_and_b32_e32 v103, 0xffff0000, v40
	v_lshlrev_b32_e32 v104, 16, v41
	v_and_b32_e32 v105, 0xffff0000, v41
	s_waitcnt vmcnt(16)
	v_lshlrev_b32_e32 v40, 16, v32
	v_and_b32_e32 v41, 0xffff0000, v32
	v_pk_fma_f32 v[108:109], v[0:1], v[42:43], 0 op_sel_hi:[0,1,0]
	v_pk_fma_f32 v[110:111], v[0:1], v[40:41], 0 op_sel_hi:[0,1,0]
	global_load_dwordx4 v[40:43], v[78:79], off offset:3072
	s_waitcnt vmcnt(15)
	v_lshlrev_b32_e32 v82, 16, v54
	v_and_b32_e32 v83, 0xffff0000, v54
	v_lshlrev_b32_e32 v54, 16, v55
	v_and_b32_e32 v55, 0xffff0000, v55
	s_waitcnt vmcnt(14)
	v_lshlrev_b32_e32 v96, 16, v44
	v_and_b32_e32 v97, 0xffff0000, v44
	v_lshlrev_b32_e32 v44, 16, v45
	v_and_b32_e32 v45, 0xffff0000, v45
	v_pk_fma_f32 v[80:81], v[0:1], v[80:81], 0 op_sel_hi:[0,1,0]
	v_pk_fma_f32 v[88:89], v[0:1], v[88:89], 0 op_sel_hi:[0,1,0]
	v_pk_fma_f32 v[94:95], v[0:1], v[94:95], 0 op_sel_hi:[0,1,0]
	s_waitcnt vmcnt(11)
	v_lshlrev_b32_e32 v84, 16, v56
	v_and_b32_e32 v85, 0xffff0000, v56
	v_lshlrev_b32_e32 v56, 16, v57
	v_and_b32_e32 v57, 0xffff0000, v57
	s_waitcnt vmcnt(10)
	v_lshlrev_b32_e32 v98, 16, v46
	v_and_b32_e32 v99, 0xffff0000, v46
	v_lshlrev_b32_e32 v46, 16, v47
	v_and_b32_e32 v47, 0xffff0000, v47
	v_pk_fma_f32 v[80:81], v[0:1], v[82:83], v[80:81] op_sel:[1,0,0]
	v_pk_fma_f32 v[54:55], v[0:1], v[54:55], v[88:89] op_sel:[1,0,0]
	v_pk_fma_f32 v[78:79], v[0:1], v[96:97], v[94:95] op_sel:[1,0,0]
	v_pk_fma_f32 v[44:45], v[0:1], v[44:45], v[108:109] op_sel:[1,0,0]
	s_waitcnt vmcnt(7)
	v_lshlrev_b32_e32 v86, 16, v58
	v_and_b32_e32 v87, 0xffff0000, v58
	v_lshlrev_b32_e32 v58, 16, v59
	v_and_b32_e32 v59, 0xffff0000, v59
	s_waitcnt vmcnt(6)
	v_lshlrev_b32_e32 v100, 16, v48
	v_and_b32_e32 v101, 0xffff0000, v48
	v_lshlrev_b32_e32 v48, 16, v49
	v_and_b32_e32 v49, 0xffff0000, v49
	v_pk_fma_f32 v[80:81], v[2:3], v[84:85], v[80:81] op_sel_hi:[0,1,1]
	v_pk_fma_f32 v[54:55], v[2:3], v[56:57], v[54:55] op_sel_hi:[0,1,1]
	v_pk_fma_f32 v[56:57], v[2:3], v[98:99], v[78:79] op_sel_hi:[0,1,1]
	v_pk_fma_f32 v[44:45], v[2:3], v[46:47], v[44:45] op_sel_hi:[0,1,1]
	v_pk_fma_f32 v[46:47], v[2:3], v[86:87], v[80:81] op_sel:[1,0,0]
	v_pk_fma_f32 v[54:55], v[2:3], v[58:59], v[54:55] op_sel:[1,0,0]
	v_pk_fma_f32 v[56:57], v[2:3], v[100:101], v[56:57] op_sel:[1,0,0]
	v_pk_fma_f32 v[44:45], v[2:3], v[48:49], v[44:45] op_sel:[1,0,0]
	v_lshlrev_b32_e32 v32, 16, v33
	v_and_b32_e32 v33, 0xffff0000, v33
	v_lshlrev_b32_e32 v106, 16, v34
	v_and_b32_e32 v107, 0xffff0000, v34
	v_pk_fma_f32 v[32:33], v[0:1], v[32:33], 0 op_sel_hi:[0,1,0]
	v_lshlrev_b32_e32 v34, 16, v35
	v_and_b32_e32 v35, 0xffff0000, v35
	v_pk_fma_f32 v[32:33], v[0:1], v[34:35], v[32:33] op_sel:[1,0,0]
	v_lshlrev_b32_e32 v34, 16, v37
	v_and_b32_e32 v35, 0xffff0000, v37
	v_pk_fma_f32 v[32:33], v[2:3], v[34:35], v[32:33] op_sel_hi:[0,1,1]
	s_waitcnt vmcnt(5)
	v_lshlrev_b32_e32 v34, 16, v39
	v_and_b32_e32 v35, 0xffff0000, v39
	v_pk_fma_f32 v[32:33], v[2:3], v[34:35], v[32:33] op_sel:[1,0,0]
	v_lshlrev_b32_e32 v34, 16, v30
	v_and_b32_e32 v35, 0xffff0000, v30
	v_lshlrev_b32_e32 v30, 16, v31
	s_waitcnt vmcnt(3)
	v_pk_fma_f32 v[48:49], v[54:55], v[72:73], v[92:93]
	v_pk_fma_f32 v[46:47], v[46:47], v[70:71], v[90:91]
	s_waitcnt vmcnt(2)
	v_pk_fma_f32 v[44:45], v[44:45], v[76:77], v[104:105]
	v_pk_fma_f32 v[54:55], v[56:57], v[74:75], v[102:103]
	v_pk_mul_f32 v[56:57], v[46:47], v[46:47]
	v_pk_mul_f32 v[58:59], v[48:49], v[48:49]
	v_pk_mul_f32 v[70:71], v[44:45], v[44:45]
	v_pk_mul_f32 v[72:73], v[54:55], v[54:55]
	v_pk_mov_b32 v[74:75], v[56:57], v[58:59] op_sel:[1,0]
	v_mov_b32_e32 v57, v59
	v_pk_mov_b32 v[58:59], v[72:73], v[70:71] op_sel:[1,0]
	v_mov_b32_e32 v73, v71
	v_pk_add_f32 v[58:59], v[58:59], v[72:73]
	v_pk_fma_f32 v[70:71], v[0:1], v[106:107], v[110:111] op_sel:[1,0,0]
	v_lshlrev_b32_e32 v72, 16, v36
	v_and_b32_e32 v73, 0xffff0000, v36
	v_pk_fma_f32 v[70:71], v[2:3], v[72:73], v[70:71] op_sel_hi:[0,1,1]
	v_lshlrev_b32_e32 v72, 16, v38
	v_and_b32_e32 v73, 0xffff0000, v38
	v_pk_fma_f32 v[70:71], v[2:3], v[72:73], v[70:71] op_sel:[1,0,0]
	v_and_b32_e32 v31, 0xffff0000, v31
	s_waitcnt vmcnt(1)
; __device__ __forceinline__ float bflo(unsigned w) { return __uint_as_float(w << 16); }
; __device__ __forceinline__ float bfhi(unsigned w) { return __uint_as_float(w & 0xffff0000u); }
; __device__ __forceinline__ void p_final(const Args& a, const Frame& F, int half) {
;     ...
;         f32x4 v[4]; float s = 0.f;
; #pragma unroll
;         for (int j = 0; j < 4; ++j) {
;             f32x4 m = (f32x4){0.f, 0.f, 0.f, 0.f};
; #pragma unroll
;             for (int k = 0; k < 4; ++k) { const u32x2 o = ok[j][k]; m.x += wk[k] * bflo(o.x); m.y += wk[k] * bfhi(o.x); m.z += wk[k] * bflo(o.y); m.w += wk[k] * bfhi(o.y); }
;             v[j] = (f32x4){bflo(xw[j].x), bfhi(xw[j].x), bflo(xw[j].y), bfhi(xw[j].y)} + g2[64 * j] * m;
;             s += (v[j].x * v[j].x + v[j].y * v[j].y) + (v[j].z * v[j].z + v[j].w * v[j].w);
;         }
;         const float rstd = rsqrtf(wave_sum(s) * (1.f / D) + EPS);
; #pragma unroll
;         for (int j = 0; j < 4; ++j) xr[64 * j] = v[j] * rstd * fw[64 * j];
	v_pk_fma_f32 v[30:31], v[32:33], v[52:53], v[30:31]
	v_pk_fma_f32 v[32:33], v[70:71], v[50:51], v[34:35]
	v_lshlrev_b32_e32 v34, 16, v26
	v_and_b32_e32 v35, 0xffff0000, v26
	v_pk_fma_f32 v[34:35], v[0:1], v[34:35], 0 op_sel_hi:[0,1,0]
	v_lshlrev_b32_e32 v36, 16, v28
	v_and_b32_e32 v37, 0xffff0000, v28
	v_pk_fma_f32 v[34:35], v[0:1], v[36:37], v[34:35] op_sel:[1,0,0]
	v_lshlrev_b32_e32 v36, 16, v22
	v_and_b32_e32 v37, 0xffff0000, v22
	v_pk_fma_f32 v[34:35], v[2:3], v[36:37], v[34:35] op_sel_hi:[0,1,1]
	v_lshlrev_b32_e32 v36, 16, v24
	v_and_b32_e32 v37, 0xffff0000, v24
	v_lshlrev_b32_e32 v26, 16, v27
	v_and_b32_e32 v27, 0xffff0000, v27
	v_pk_fma_f32 v[34:35], v[2:3], v[36:37], v[34:35] op_sel:[1,0,0]
	v_pk_fma_f32 v[36:37], v[0:1], v[26:27], 0 op_sel_hi:[0,1,0]
	v_lshlrev_b32_e32 v38, 16, v29
	v_and_b32_e32 v39, 0xffff0000, v29
	v_pk_fma_f32 v[0:1], v[0:1], v[38:39], v[36:37] op_sel:[1,0,0]
	v_lshlrev_b32_e32 v22, 16, v23
	v_and_b32_e32 v23, 0xffff0000, v23
	v_pk_fma_f32 v[0:1], v[2:3], v[22:23], v[0:1] op_sel_hi:[0,1,1]
	v_lshlrev_b32_e32 v22, 16, v25
	v_and_b32_e32 v23, 0xffff0000, v25
	v_pk_fma_f32 v[0:1], v[2:3], v[22:23], v[0:1] op_sel:[1,0,0]
	v_lshlrev_b32_e32 v2, 16, v20
	v_and_b32_e32 v3, 0xffff0000, v20
	v_pk_add_f32 v[56:57], v[74:75], v[56:57]
	v_lshlrev_b32_e32 v20, 16, v21
	v_and_b32_e32 v21, 0xffff0000, v21
	s_waitcnt vmcnt(0)
	v_pk_fma_f32 v[34:35], v[34:35], v[40:41], v[2:3]
	v_pk_fma_f32 v[24:25], v[0:1], v[42:43], v[20:21]
	v_mul_f32_e32 v2, v34, v34
	v_pk_add_f32 v[0:1], v[56:57], v[56:57] op_sel:[0,1] op_sel_hi:[1,0]
	v_mul_f32_e32 v4, v35, v35
	v_mov_b32_e32 v1, v2
	v_pk_add_f32 v[2:3], v[58:59], v[58:59] op_sel:[0,1] op_sel_hi:[1,0]
	v_mul_f32_e32 v20, v24, v24
	v_mov_b32_e32 v3, v4
	v_pk_add_f32 v[0:1], v[0:1], v[2:3]
	v_mul_f32_e32 v2, v33, v33
	v_pk_fma_f32 v[2:3], v[32:33], v[32:33], v[2:3] op_sel_hi:[1,1,0]
	v_mul_f32_e32 v4, v31, v31
	v_mul_f32_e32 v22, v25, v25
	v_mov_b32_e32 v3, v20
	v_pk_fma_f32 v[20:21], v[30:31], v[30:31], v[4:5] op_sel_hi:[1,1,0]
	s_add_u32 s0, s0, s2
	v_mov_b32_e32 v21, v22
	v_pk_add_f32 v[2:3], v[2:3], v[20:21]
	s_addc_u32 s1, s1, s3
	v_pk_add_f32 v[0:1], v[0:1], v[2:3]
	s_add_i32 s6, s6, s19
	v_add_f32_e32 v0, v0, v1
	s_cmp_lt_i32 s0, 0x10000
	s_nop 1
	v_add_f32_dpp v0, v0, v0 row_ror:8 row_mask:0xf bank_mask:0xf bound_ctrl:1
	s_nop 1
	v_add_f32_dpp v0, v0, v0 row_ror:4 row_mask:0xf bank_mask:0xf bound_ctrl:1
	s_nop 1
	v_add_f32_dpp v0, v0, v0 row_ror:2 row_mask:0xf bank_mask:0xf bound_ctrl:1
	s_nop 1
	v_add_f32_dpp v0, v0, v0 row_ror:1 row_mask:0xf bank_mask:0xf bound_ctrl:1
	s_nop 1
	v_mov_b32_e32 v1, v0
	s_nop 1
	v_permlane16_swap_b32_e32 v0, v1
	s_nop 1
	v_add_f32_e32 v0, v0, v1
	v_mov_b32_e32 v1, v0
	s_nop 1
	v_permlane32_swap_b32_e32 v0, v1
	s_nop 1
	v_add_f32_e32 v0, v0, v1
	v_fmamk_f32 v0, v0, 0x3a800000, v68
	v_mul_f32_e32 v1, 0x4b800000, v0
	v_cmp_gt_f32_e32 vcc, s20, v0
	s_nop 1
	v_cndmask_b32_e32 v0, v0, v1, vcc
	v_rsq_f32_e32 v0, v0
	s_nop 0
	v_mul_f32_e32 v1, 0x45800000, v0
	v_cndmask_b32_e32 v4, v0, v1, vcc
	v_pk_mul_f32 v[0:1], v[46:47], v[4:5] op_sel_hi:[1,0]
	v_pk_mul_f32 v[2:3], v[48:49], v[4:5] op_sel_hi:[1,0]
	s_waitcnt vmcnt(0)
	v_pk_mul_f32 v[0:1], v[120:121], v[0:1]
	v_pk_mul_f32 v[2:3], v[122:123], v[2:3]
	global_store_dwordx4 v[10:11], v[0:3], off offset:-3072 nt
	v_pk_mul_f32 v[20:21], v[44:45], v[4:5] op_sel_hi:[1,0]
	v_pk_mul_f32 v[22:23], v[54:55], v[4:5] op_sel_hi:[1,0]
	v_pk_mul_f32 v[2:3], v[126:127], v[20:21]
	v_pk_mul_f32 v[0:1], v[124:125], v[22:23]
	global_store_dwordx4 v[10:11], v[0:3], off offset:-2048 nt
	v_pk_mul_f32 v[20:21], v[30:31], v[4:5] op_sel_hi:[1,0]
	v_pk_mul_f32 v[22:23], v[32:33], v[4:5] op_sel_hi:[1,0]
	v_pk_mul_f32 v[2:3], v[130:131], v[20:21]
	v_pk_mul_f32 v[0:1], v[128:129], v[22:23]
	global_store_dwordx4 v[10:11], v[0:3], off offset:-1024 nt
	s_nop 1
	v_mov_b64_e32 v[0:1], v[18:19]
	v_pk_mul_f32 v[2:3], v[24:25], v[4:5] op_sel_hi:[1,0]
	v_pk_mul_f32 v[18:19], v[34:35], v[4:5] op_sel_hi:[1,0]
	v_pk_mul_f32 v[18:19], v[132:133], v[18:19]
	v_pk_mul_f32 v[20:21], v[134:135], v[2:3]
	global_store_dwordx4 v[10:11], v[18:21], off nt
	v_lshl_add_u64 v[10:11], v[10:11], 0, s[8:9]
	v_mov_b64_e32 v[2:3], v[16:17]
	s_cbranch_scc0 .LBB0_1398
